# gb1: grid barrier (per-layer sites): waiting workgroups poll the global generation word directly instead of their XCD's forwarded copy (one hop less); on top of rt1
# speedup vs baseline: 1.0023x; 1.0014x over previous
; __device__ __forceinline__ unsigned xb_ld(unsigned* p)              { return __hip_atomic_load(p, __ATOMIC_RELAXED, __HIP_MEMORY_SCOPE_AGENT); }
; __device__ __forceinline__ unsigned xb_add(unsigned* p, unsigned v) { return __hip_atomic_fetch_add(p, v, __ATOMIC_RELAXED, __HIP_MEMORY_SCOPE_AGENT); }
; #define XB_SPIN(cond, bar) do { unsigned _sp = 0; while (cond) { __builtin_amdgcn_s_sleep(1); \
;     if ((++_sp & 255u) == 0u) { if (xb_ld(&(bar)[XB_TMO])) break; if (_sp > XB_SPIN_CAP) { atomicAdd(&(bar)[XB_TMO], 1u); break; } } } } while (0)
; __device__ __forceinline__ void xcd_barrier(const XcdBarrier& b) {
;     ...
;         const unsigned old = xb_add(&bar[XB_XSUB(bx_)], 1u);
;         const unsigned gen = old / nloc;
;         if (old + 1u == (gen + 1u) * nloc) {
;             __builtin_amdgcn_fence(__ATOMIC_RELEASE, "agent");
;             asm volatile("s_waitcnt vmcnt(0)" ::: "memory");
;             const unsigned og = xb_add(&bar[XB_TOP], 1u);
;             const unsigned tg = og / nx;
;             if (og + 1u == (tg + 1u) * nx) xb_add(&bar[XB_TOPGEN], 1u);
;             else XB_SPIN(xb_ld(&bar[XB_TOPGEN]) == tg, bar);
;             __builtin_amdgcn_fence(__ATOMIC_ACQUIRE, "agent");
;             xb_add(&bar[XB_XGEN(bx_)], 1u);
;             asm volatile("s_waitcnt vmcnt(0)" ::: "memory");
;         } else {
;             XB_SPIN(xb_ld(&bar[XB_XGEN(bx_)]) == gen, bar);
.LBB0_771:
	s_lshl_b32 s2, s2, 6
	s_add_i32 s64, s2, 0x500
	s_lshl_b64 s[0:1], s[64:65], 2
	s_add_u32 s0, s38, s0
	s_addc_u32 s1, s39, s1
	v_mov_b64_e32 v[4:5], s[0:1]
	flat_atomic_add v3, v[4:5], v249 sc0
	v_cvt_f32_u32_e32 v1, v2
	v_sub_u32_e32 v4, 0, v2
	v_rcp_iflag_f32_e32 v1, v1
	s_nop 0
	v_mul_f32_e32 v1, 0x4f7ffffe, v1
	v_cvt_u32_f32_e32 v1, v1
	v_mul_lo_u32 v4, v4, v1
	v_mul_hi_u32 v4, v1, v4
	v_add_u32_e32 v1, v1, v4
	s_waitcnt vmcnt(0) lgkmcnt(0)
	v_mul_hi_u32 v1, v3, v1
	v_mul_lo_u32 v4, v1, v2
	v_sub_u32_e32 v4, v3, v4
	v_cmp_ge_u32_e32 vcc, v4, v2
	v_add_u32_e32 v5, 1, v1
	s_nop 0
	v_cndmask_b32_e32 v1, v1, v5, vcc
	v_sub_u32_e32 v5, v4, v2
	v_cndmask_b32_e32 v4, v4, v5, vcc
	v_cmp_ge_u32_e32 vcc, v4, v2
	v_add_u32_e32 v4, 1, v1
	s_nop 0
	v_cndmask_b32_e32 v1, v1, v4, vcc
	v_add_u32_e32 v4, 1, v3
	v_mad_u64_u32 v[2:3], s[0:1], v2, v1, v[2:3]
	v_cmp_ne_u32_e32 vcc, v4, v2
	s_and_saveexec_b64 s[0:1], vcc
	s_xor_b64 s[0:1], exec, s[0:1]
	s_cbranch_execz .LBB0_784
	s_add_i32 s64, s2, 0x900
	s_add_u32 s6, s38, 0x3500
	s_addc_u32 s7, s39, 0
	v_mov_b64_e32 v[2:3], s[6:7]
	flat_load_dword v0, v[2:3] sc1
	s_waitcnt vmcnt(0) lgkmcnt(0)
	v_cmp_eq_u32_e32 vcc, v0, v1
	s_and_saveexec_b64 s[4:5], vcc
	s_cbranch_execz .LBB0_783
	s_mov_b32 s3, 1
	s_mov_b64 s[10:11], 0
	s_branch .LBB0_775
